# v19 plus per-edge scale broadcast via permlane16_swap instead of two ds_bpermute
# speedup vs baseline: 1.0044x; 1.0022x over previous
.LBB1_6:
	s_waitcnt vmcnt(14)
	ds_write_b128 v119, v[38:41]
	s_waitcnt vmcnt(13)
	ds_write_b128 v119, v[42:45] offset:2304
	s_waitcnt vmcnt(12)
	ds_write_b128 v119, v[46:49] offset:4608
	s_waitcnt vmcnt(11)
	ds_write_b128 v119, v[50:53] offset:6912
	ds_bpermute_b32 v42, v107, v64
	ds_bpermute_b32 v43, v109, v64
	ds_bpermute_b32 v44, v110, v64
	v_add_u32_e32 v0, 0x1000, v62
	ds_bpermute_b32 v50, v111, v64
	v_min_i32_e32 v0, 0x927b, v0
	v_lshl_or_b32 v40, v0, 4, v106
	s_waitcnt lgkmcnt(3)
	v_lshlrev_b32_e32 v0, 7, v42
	v_ashrrev_i32_e32 v65, 31, v64
	v_lshl_add_u64 v[46:47], v[98:99], 0, v[0:1]
	s_waitcnt lgkmcnt(2)
	v_lshlrev_b32_e32 v0, 7, v43
	v_lshl_add_u64 v[38:39], v[64:65], 2, v[96:97]
	v_ashrrev_i32_e32 v41, 31, v40
	v_lshl_add_u64 v[48:49], v[98:99], 0, v[0:1]
	s_waitcnt lgkmcnt(1)
	v_lshlrev_b32_e32 v0, 7, v44
	s_waitcnt vmcnt(10)
	v_mov_b32_e32 v68, v108
	v_mov_b32_e32 v66, v108
	s_nop 1
	v_permlane16_swap_b32_e32 v68, v66
	global_load_dword v108, v[38:39], off
	v_lshl_add_u64 v[38:39], v[40:41], 2, v[94:95]
	v_lshl_add_u64 v[64:65], v[100:101], 0, v[0:1]
	s_waitcnt lgkmcnt(0)
	v_lshlrev_b32_e32 v0, 7, v50
	global_load_dword v135, v[38:39], off
	s_nop 0
	global_load_dwordx4 v[38:41], v[46:47], off
	global_load_dwordx4 v[42:45], v[48:49], off
	v_lshl_add_u64 v[70:71], v[100:101], 0, v[0:1]
	global_load_dwordx4 v[46:49], v[64:65], off
	global_load_dwordx4 v[50:53], v[70:71], off
	ds_read_b128 v[70:73], v120
	ds_read_b128 v[74:77], v120 offset:64
	ds_read_b128 v[78:81], v120 offset:4608
	ds_read_b128 v[82:85], v120 offset:4672
	v_add_u32_e32 v0, 0x800, v62
	ds_write_b128 v121, v[2:5]
	ds_write_b128 v121, v[6:9] offset:1088
	ds_write_b128 v121, v[10:13] offset:2176
	ds_write_b128 v121, v[14:17] offset:3264
	ds_write_b128 v121, v[18:21] offset:4352
	ds_write_b128 v121, v[22:25] offset:5440
	s_waitcnt vmcnt(15)
	ds_write_b128 v121, v[26:29] offset:6528
	s_waitcnt vmcnt(14)
	ds_write_b128 v121, v[30:33] offset:7616
	ds_write_b128 v122, v[34:37] offset:8704
	v_min_i32_e32 v2, 0x927b, v0
	v_ashrrev_i32_e32 v3, 31, v2
	v_lshlrev_b64 v[4:5], 13, v[2:3]
	v_lshlrev_b64 v[2:3], 10, v[2:3]
	v_lshl_add_u64 v[18:19], v[102:103], 0, v[4:5]
	v_lshl_add_u64 v[62:63], v[104:105], 0, v[2:3]
	v_add_co_u32_e32 v64, vcc, s3, v18
	global_load_dwordx4 v[2:5], v[18:19], off nt
	global_load_dwordx4 v[6:9], v[18:19], off offset:1024 nt
	global_load_dwordx4 v[10:13], v[18:19], off offset:2048 nt
	global_load_dwordx4 v[14:17], v[18:19], off offset:3072 nt
	v_addc_co_u32_e32 v65, vcc, 0, v19, vcc
	global_load_dwordx4 v[34:37], v[62:63], off nt
	global_load_dwordx4 v[18:21], v[64:65], off nt
	global_load_dwordx4 v[22:25], v[64:65], off offset:1024 nt
	global_load_dwordx4 v[26:29], v[64:65], off offset:2048 nt
	global_load_dwordx4 v[30:33], v[64:65], off offset:3072 nt
	s_waitcnt lgkmcnt(13)
	v_add_f32_e32 v67, v68, v66
	v_mul_f32_e32 v184, 0xc3000000, v67
	s_waitcnt lgkmcnt(12)
	v_cvt_f32_ubyte3_e32 v169, v70
	v_cvt_f32_ubyte2_e32 v168, v70
	v_cvt_f32_ubyte1_e32 v171, v70
	v_cvt_f32_ubyte0_e32 v170, v70
	ds_read_b128 v[62:65], v123
	ds_read_b128 v[86:89], v123 offset:64
	ds_read_b128 v[90:93], v112
	ds_read_b128 v[136:139], v112 offset:4608
	ds_read_b128 v[140:143], v112 offset:9216
	ds_read_b128 v[144:147], v112 offset:13824
	ds_read_b128 v[148:151], v112 offset:18432
	ds_read_b128 v[152:155], v112 offset:23040
	ds_read_b128 v[156:159], v112 offset:27648
	ds_read_b128 v[160:163], v112 offset:32256
	s_waitcnt lgkmcnt(14)
	v_cvt_f32_ubyte1_e32 v165, v78
	v_cvt_f32_ubyte0_e32 v164, v78
	v_cvt_f32_ubyte3_e32 v167, v78
	v_cvt_f32_ubyte2_e32 v166, v78
	v_pk_fma_f32 v[170:171], v[170:171], v[68:69], v[184:185] op_sel_hi:[1,0,0]
	v_pk_fma_f32 v[168:169], v[168:169], v[68:69], v[184:185] op_sel_hi:[1,0,0]
	v_pk_fma_f32 v[164:165], v[164:165], v[66:67], v[170:171] op_sel_hi:[1,0,1]
	v_pk_fma_f32 v[166:167], v[166:167], v[66:67], v[168:169] op_sel_hi:[1,0,1]
	v_cvt_f32_ubyte1_e32 v169, v79
	v_cvt_f32_ubyte0_e32 v168, v79
	v_cvt_f32_ubyte3_e32 v171, v79
	v_cvt_f32_ubyte2_e32 v170, v79
	v_cvt_f32_ubyte3_e32 v79, v71
	v_cvt_f32_ubyte2_e32 v78, v71
	v_cvt_f32_ubyte1_e32 v173, v71
	v_cvt_f32_ubyte0_e32 v172, v71
	v_pk_fma_f32 v[70:71], v[172:173], v[68:69], v[184:185] op_sel_hi:[1,0,0]
	v_pk_fma_f32 v[78:79], v[78:79], v[68:69], v[184:185] op_sel_hi:[1,0,0]
	v_cvt_f32_ubyte3_e32 v173, v72
	v_cvt_f32_ubyte2_e32 v172, v72
	v_cvt_f32_ubyte1_e32 v175, v72
	v_cvt_f32_ubyte0_e32 v174, v72
	v_pk_fma_f32 v[170:171], v[170:171], v[66:67], v[78:79] op_sel_hi:[1,0,1]
	v_pk_fma_f32 v[168:169], v[168:169], v[66:67], v[70:71] op_sel_hi:[1,0,1]
	v_cvt_f32_ubyte1_e32 v71, v80
	v_cvt_f32_ubyte0_e32 v70, v80
	v_cvt_f32_ubyte3_e32 v79, v80
	v_cvt_f32_ubyte2_e32 v78, v80
	v_pk_fma_f32 v[176:177], v[174:175], v[68:69], v[184:185] op_sel_hi:[1,0,0]
	v_pk_fma_f32 v[172:173], v[172:173], v[68:69], v[184:185] op_sel_hi:[1,0,0]
	v_cvt_f32_ubyte2_e32 v80, v73
	v_pk_fma_f32 v[174:175], v[78:79], v[66:67], v[172:173] op_sel_hi:[1,0,1]
	v_pk_fma_f32 v[172:173], v[70:71], v[66:67], v[176:177] op_sel_hi:[1,0,1]
	v_cvt_f32_ubyte1_e32 v177, v73
	v_cvt_f32_ubyte0_e32 v176, v73
	v_cvt_f32_ubyte1_e32 v71, v81
	v_cvt_f32_ubyte0_e32 v70, v81
	v_cvt_f32_ubyte3_e32 v79, v81
	v_cvt_f32_ubyte2_e32 v78, v81
	v_cvt_f32_ubyte3_e32 v81, v73
	v_pk_fma_f32 v[176:177], v[176:177], v[68:69], v[184:185] op_sel_hi:[1,0,0]
	v_pk_fma_f32 v[72:73], v[80:81], v[68:69], v[184:185] op_sel_hi:[1,0,0]
	v_pk_fma_f32 v[70:71], v[70:71], v[66:67], v[176:177] op_sel_hi:[1,0,1]
	v_cvt_f32_ubyte3_e32 v177, v74
	v_cvt_f32_ubyte2_e32 v176, v74
	v_cvt_f32_ubyte1_e32 v179, v74
	v_cvt_f32_ubyte0_e32 v178, v74
	v_pk_fma_f32 v[72:73], v[78:79], v[66:67], v[72:73] op_sel_hi:[1,0,1]
	v_cvt_f32_ubyte1_e32 v79, v82
	v_cvt_f32_ubyte0_e32 v78, v82
	v_cvt_f32_ubyte3_e32 v81, v82
	v_cvt_f32_ubyte2_e32 v80, v82
	v_pk_fma_f32 v[178:179], v[178:179], v[68:69], v[184:185] op_sel_hi:[1,0,0]
	v_pk_fma_f32 v[176:177], v[176:177], v[68:69], v[184:185] op_sel_hi:[1,0,0]
	v_pk_fma_f32 v[78:79], v[78:79], v[66:67], v[178:179] op_sel_hi:[1,0,1]
	v_pk_fma_f32 v[80:81], v[80:81], v[66:67], v[176:177] op_sel_hi:[1,0,1]
	v_cvt_f32_ubyte1_e32 v177, v83
	v_cvt_f32_ubyte0_e32 v176, v83
	v_cvt_f32_ubyte3_e32 v179, v83
	v_cvt_f32_ubyte2_e32 v178, v83
	v_cvt_f32_ubyte3_e32 v83, v75
	v_cvt_f32_ubyte2_e32 v82, v75
	v_cvt_f32_ubyte1_e32 v181, v75
	v_cvt_f32_ubyte0_e32 v180, v75
	v_pk_fma_f32 v[74:75], v[180:181], v[68:69], v[184:185] op_sel_hi:[1,0,0]
	v_pk_fma_f32 v[82:83], v[82:83], v[68:69], v[184:185] op_sel_hi:[1,0,0]
	v_cvt_f32_ubyte3_e32 v181, v76
	v_cvt_f32_ubyte2_e32 v180, v76
	v_cvt_f32_ubyte1_e32 v183, v76
	v_cvt_f32_ubyte0_e32 v182, v76
	v_pk_fma_f32 v[178:179], v[178:179], v[66:67], v[82:83] op_sel_hi:[1,0,1]
	v_pk_fma_f32 v[176:177], v[176:177], v[66:67], v[74:75] op_sel_hi:[1,0,1]
	v_cvt_f32_ubyte1_e32 v75, v84
	v_cvt_f32_ubyte0_e32 v74, v84
	v_cvt_f32_ubyte3_e32 v83, v84
	v_cvt_f32_ubyte2_e32 v82, v84
	v_pk_fma_f32 v[186:187], v[182:183], v[68:69], v[184:185] op_sel_hi:[1,0,0]
	v_pk_fma_f32 v[180:181], v[180:181], v[68:69], v[184:185] op_sel_hi:[1,0,0]
	v_cvt_f32_ubyte2_e32 v84, v77
	v_pk_fma_f32 v[182:183], v[82:83], v[66:67], v[180:181] op_sel_hi:[1,0,1]
	v_pk_fma_f32 v[180:181], v[74:75], v[66:67], v[186:187] op_sel_hi:[1,0,1]
	v_cvt_f32_ubyte1_e32 v75, v85
	v_cvt_f32_ubyte0_e32 v74, v85
	v_cvt_f32_ubyte3_e32 v83, v85
	v_cvt_f32_ubyte2_e32 v82, v85
	v_cvt_f32_ubyte3_e32 v85, v77
	v_cvt_f32_ubyte1_e32 v187, v77
	v_cvt_f32_ubyte0_e32 v186, v77
	v_pk_fma_f32 v[76:77], v[186:187], v[68:69], v[184:185] op_sel_hi:[1,0,0]
	v_pk_fma_f32 v[68:69], v[84:85], v[68:69], v[184:185] op_sel_hi:[1,0,0]
	s_nop 0
	v_pk_fma_f32 v[68:69], v[82:83], v[66:67], v[68:69] op_sel_hi:[1,0,1]
	v_pk_fma_f32 v[66:67], v[74:75], v[66:67], v[76:77] op_sel_hi:[1,0,1]
	ds_read_b128 v[74:77], v123 offset:128
	ds_read_b128 v[82:85], v123 offset:192
	ds_read_b128 v[184:187], v112 offset:64
	ds_read_b128 v[188:191], v112 offset:4672
	ds_read_b128 v[192:195], v112 offset:9280
	ds_read_b128 v[196:199], v112 offset:13888
	ds_read_b128 v[200:203], v112 offset:18496
	ds_read_b128 v[204:207], v112 offset:23104
	ds_read_b128 v[208:211], v112 offset:27712
	ds_read_b128 v[212:215], v112 offset:32320
	s_waitcnt lgkmcnt(14)
	v_cvt_pk_bf16_f32 v62, v62, v63
	v_cvt_pk_bf16_f32 v63, v64, v65
	v_cvt_pk_bf16_f32 v64, v86, v87
	v_cvt_pk_bf16_f32 v65, v88, v89
	s_nop 1
	v_mfma_f32_16x16x32_bf16 v[86:89], v[90:93], v[62:65], v[164:167]
	v_mfma_f32_16x16x32_bf16 v[90:93], v[136:139], v[62:65], v[168:171]
	v_mfma_f32_16x16x32_bf16 v[136:139], v[140:143], v[62:65], v[172:175]
	v_mfma_f32_16x16x32_bf16 v[70:73], v[144:147], v[62:65], v[70:73]
	s_waitcnt lgkmcnt(13)
	v_mfma_f32_16x16x32_bf16 v[78:81], v[148:151], v[62:65], v[78:81]
	s_waitcnt lgkmcnt(12)
	v_mfma_f32_16x16x32_bf16 v[140:143], v[152:155], v[62:65], v[176:179]
	s_waitcnt lgkmcnt(11)
	v_mfma_f32_16x16x32_bf16 v[144:147], v[156:159], v[62:65], v[180:183]
	s_waitcnt lgkmcnt(10)
	v_mfma_f32_16x16x32_bf16 v[62:65], v[160:163], v[62:65], v[66:69]
	s_nop 2
	ds_read_b128 v[66:69], v123 offset:256
	ds_read_b128 v[148:151], v123 offset:320
	ds_read_b128 v[152:155], v112 offset:128
	ds_read_b128 v[156:159], v112 offset:4736
	ds_read_b128 v[160:163], v112 offset:9344
	ds_read_b128 v[164:167], v112 offset:13952
	ds_read_b128 v[168:171], v112 offset:18560
	ds_read_b128 v[172:175], v112 offset:23168
	ds_read_b128 v[176:179], v112 offset:27776
	ds_read_b128 v[180:183], v112 offset:32384
	s_waitcnt lgkmcnt(14)
	v_cvt_pk_bf16_f32 v74, v74, v75
	v_cvt_pk_bf16_f32 v75, v76, v77
	v_cvt_pk_bf16_f32 v76, v82, v83
	v_cvt_pk_bf16_f32 v77, v84, v85
	s_waitcnt lgkmcnt(10)
	s_nop 0
	v_mfma_f32_16x16x32_bf16 v[62:65], v[212:215], v[74:77], v[62:65]
	v_mfma_f32_16x16x32_bf16 v[82:85], v[184:187], v[74:77], v[86:89]
	v_mfma_f32_16x16x32_bf16 v[86:89], v[188:191], v[74:77], v[90:93]
	v_mfma_f32_16x16x32_bf16 v[90:93], v[192:195], v[74:77], v[136:139]
	v_mfma_f32_16x16x32_bf16 v[70:73], v[196:199], v[74:77], v[70:73]
	v_mfma_f32_16x16x32_bf16 v[78:81], v[200:203], v[74:77], v[78:81]
	v_mfma_f32_16x16x32_bf16 v[136:139], v[204:207], v[74:77], v[140:143]
	v_mfma_f32_16x16x32_bf16 v[140:143], v[208:211], v[74:77], v[144:147]
	ds_read_b128 v[74:77], v123 offset:384
	s_nop 1
	ds_read_b128 v[144:147], v123 offset:448
	ds_read_b128 v[184:187], v112 offset:192
	ds_read_b128 v[188:191], v112 offset:4800
	ds_read_b128 v[192:195], v112 offset:9408
	ds_read_b128 v[196:199], v112 offset:14016
	ds_read_b128 v[200:203], v112 offset:18624
	ds_read_b128 v[204:207], v112 offset:23232
	ds_read_b128 v[208:211], v112 offset:27840
	ds_read_b128 v[212:215], v112 offset:32448
	s_waitcnt lgkmcnt(14)
	v_cvt_pk_bf16_f32 v66, v66, v67
	v_cvt_pk_bf16_f32 v67, v68, v69
	v_cvt_pk_bf16_f32 v68, v148, v149
	v_cvt_pk_bf16_f32 v69, v150, v151
	s_waitcnt lgkmcnt(10)
	s_nop 0
	v_mfma_f32_16x16x32_bf16 v[62:65], v[180:183], v[66:69], v[62:65]
	v_mfma_f32_16x16x32_bf16 v[82:85], v[152:155], v[66:69], v[82:85]
	v_mfma_f32_16x16x32_bf16 v[86:89], v[156:159], v[66:69], v[86:89]
	v_mfma_f32_16x16x32_bf16 v[90:93], v[160:163], v[66:69], v[90:93]
	v_mfma_f32_16x16x32_bf16 v[70:73], v[164:167], v[66:69], v[70:73]
	v_mfma_f32_16x16x32_bf16 v[78:81], v[168:171], v[66:69], v[78:81]
	v_mfma_f32_16x16x32_bf16 v[136:139], v[172:175], v[66:69], v[136:139]
	v_mfma_f32_16x16x32_bf16 v[140:143], v[176:179], v[66:69], v[140:143]
	ds_read2st64_b64 v[66:69], v134 offset0:54 offset1:63
	ds_read2st64_b64 v[148:151], v134 offset0:36 offset1:45
	ds_read2st64_b64 v[152:155], v134 offset0:18 offset1:27
	ds_read2st64_b64 v[156:159], v134 offset1:9
	ds_read_b128 v[160:163], v124 offset:8704
	s_waitcnt lgkmcnt(14)
	v_cvt_pk_bf16_f32 v74, v74, v75
	v_cvt_pk_bf16_f32 v75, v76, v77
	s_waitcnt lgkmcnt(13)
	v_cvt_pk_bf16_f32 v76, v144, v145
	v_cvt_pk_bf16_f32 v77, v146, v147
	s_waitcnt lgkmcnt(5)
	s_nop 0
	v_mfma_f32_16x16x32_bf16 v[62:65], v[212:215], v[74:77], v[62:65]
	v_mfma_f32_16x16x32_bf16 v[82:85], v[184:187], v[74:77], v[82:85]
	v_mfma_f32_16x16x32_bf16 v[86:89], v[188:191], v[74:77], v[86:89]
	v_mfma_f32_16x16x32_bf16 v[90:93], v[192:195], v[74:77], v[90:93]
	v_mfma_f32_16x16x32_bf16 v[70:73], v[196:199], v[74:77], v[70:73]
	v_mfma_f32_16x16x32_bf16 v[78:81], v[200:203], v[74:77], v[78:81]
	v_mfma_f32_16x16x32_bf16 v[136:139], v[204:207], v[74:77], v[136:139]
	v_mfma_f32_16x16x32_bf16 v[140:143], v[208:211], v[74:77], v[140:143]
	ds_read_b128 v[144:147], v125
	ds_read_b128 v[164:167], v126
	ds_read_b128 v[168:171], v127
	ds_read_b128 v[172:175], v128
	ds_read_b128 v[176:179], v129
	ds_read_b128 v[180:183], v130
	ds_read_b128 v[184:187], v131
	ds_read_b128 v[188:191], v132
	ds_read_b128 v[192:195], v112 offset:36864
	ds_read_b128 v[196:199], v112 offset:41472
	ds_read_b128 v[200:203], v112 offset:46080
	ds_read_b128 v[204:207], v112 offset:50688
	ds_read_b128 v[208:211], v112 offset:55296
	ds_read_b128 v[212:215], v112 offset:59904
	ds_read_b128 v[216:219], v112 offset:64512
	ds_read_b128 v[220:223], v113 offset:32256
	s_waitcnt lgkmcnt(14)
	v_cvt_pk_bf16_f32 v74, v160, v161
	v_cvt_pk_bf16_f32 v75, v162, v163
	s_nop 1
	v_mfma_f32_16x16x16_bf16 v[160:163], v[156:157], v[74:75], v[82:85]
	v_mfma_f32_16x16x16_bf16 v[86:89], v[158:159], v[74:75], v[86:89]
	v_mfma_f32_16x16x16_bf16 v[90:93], v[152:153], v[74:75], v[90:93]
	v_mfma_f32_16x16x16_bf16 v[70:73], v[154:155], v[74:75], v[70:73]
	v_mfma_f32_16x16x16_bf16 v[78:81], v[148:149], v[74:75], v[78:81]
	v_mfma_f32_16x16x16_bf16 v[136:139], v[150:151], v[74:75], v[136:139]
	v_mfma_f32_16x16x16_bf16 v[82:85], v[66:67], v[74:75], v[140:143]
	v_mfma_f32_16x16x16_bf16 v[74:77], v[68:69], v[74:75], v[62:65]
	s_nop 2
	v_exp_f32_e32 v62, v160
	v_exp_f32_e32 v63, v161
	v_exp_f32_e32 v64, v162
	v_exp_f32_e32 v65, v163
	v_add_f32_e32 v62, 1.0, v62
	v_add_f32_e32 v63, 1.0, v63
	v_rcp_f32_e32 v62, v62
	v_rcp_f32_e32 v63, v63
	v_add_f32_e32 v64, 1.0, v64
	v_add_f32_e32 v65, 1.0, v65
	v_rcp_f32_e32 v64, v64
	v_rcp_f32_e32 v65, v65
	v_pk_mul_f32 v[62:63], v[160:161], v[62:63]
	v_exp_f32_e32 v66, v86
	v_cvt_pk_bf16_f32 v140, v62, v63
	v_pk_mul_f32 v[62:63], v[162:163], v[64:65]
	v_exp_f32_e32 v64, v88
	v_cvt_pk_bf16_f32 v141, v62, v63
	v_exp_f32_e32 v63, v87
	v_exp_f32_e32 v65, v89
	v_add_f32_e32 v62, 1.0, v66
	v_rcp_f32_e32 v62, v62
	v_add_f32_e32 v63, 1.0, v63
	v_rcp_f32_e32 v63, v63
	v_add_f32_e32 v64, 1.0, v64
	v_add_f32_e32 v65, 1.0, v65
	v_rcp_f32_e32 v64, v64
	v_rcp_f32_e32 v65, v65
	v_pk_mul_f32 v[62:63], v[86:87], v[62:63]
	v_exp_f32_e32 v66, v90
	v_cvt_pk_bf16_f32 v142, v62, v63
	v_pk_mul_f32 v[62:63], v[88:89], v[64:65]
	v_exp_f32_e32 v64, v92
	v_cvt_pk_bf16_f32 v143, v62, v63
	v_exp_f32_e32 v63, v91
	v_exp_f32_e32 v65, v93
	v_add_f32_e32 v62, 1.0, v66
	v_rcp_f32_e32 v62, v62
	v_add_f32_e32 v63, 1.0, v63
	v_rcp_f32_e32 v63, v63
	v_add_f32_e32 v64, 1.0, v64
	v_add_f32_e32 v65, 1.0, v65
	v_rcp_f32_e32 v64, v64
	v_rcp_f32_e32 v65, v65
	v_pk_mul_f32 v[62:63], v[90:91], v[62:63]
	v_exp_f32_e32 v66, v70
	v_cvt_pk_bf16_f32 v86, v62, v63
	v_pk_mul_f32 v[62:63], v[92:93], v[64:65]
	v_exp_f32_e32 v64, v72
	v_cvt_pk_bf16_f32 v87, v62, v63
	v_exp_f32_e32 v63, v71
	v_exp_f32_e32 v65, v73
	v_add_f32_e32 v62, 1.0, v66
	v_rcp_f32_e32 v62, v62
	v_add_f32_e32 v63, 1.0, v63
	v_rcp_f32_e32 v63, v63
	v_add_f32_e32 v64, 1.0, v64
	v_add_f32_e32 v65, 1.0, v65
	v_rcp_f32_e32 v64, v64
	v_rcp_f32_e32 v65, v65
	v_pk_mul_f32 v[62:63], v[70:71], v[62:63]
	v_exp_f32_e32 v66, v78
	v_cvt_pk_bf16_f32 v88, v62, v63
	v_pk_mul_f32 v[62:63], v[72:73], v[64:65]
	v_exp_f32_e32 v64, v80
	v_cvt_pk_bf16_f32 v89, v62, v63
	v_exp_f32_e32 v63, v79
	v_exp_f32_e32 v65, v81
	v_add_f32_e32 v62, 1.0, v66
	v_rcp_f32_e32 v62, v62
	v_add_f32_e32 v63, 1.0, v63
	v_rcp_f32_e32 v63, v63
	v_add_f32_e32 v64, 1.0, v64
	v_add_f32_e32 v65, 1.0, v65
	v_rcp_f32_e32 v64, v64
	v_rcp_f32_e32 v65, v65
	v_exp_f32_e32 v66, v136
	v_pk_mul_f32 v[62:63], v[78:79], v[62:63]
	v_exp_f32_e32 v67, v139
	v_cvt_pk_bf16_f32 v148, v62, v63
	v_pk_mul_f32 v[62:63], v[80:81], v[64:65]
	v_exp_f32_e32 v65, v137
	v_add_f32_e32 v64, 1.0, v66
	v_exp_f32_e32 v66, v138
	v_rcp_f32_e32 v64, v64
	v_add_f32_e32 v65, 1.0, v65
	v_rcp_f32_e32 v65, v65
	v_add_f32_e32 v66, 1.0, v66
	v_add_f32_e32 v67, 1.0, v67
	v_rcp_f32_e32 v66, v66
	v_rcp_f32_e32 v67, v67
	v_cvt_pk_bf16_f32 v149, v62, v63
	v_pk_mul_f32 v[62:63], v[136:137], v[64:65]
	s_nop 0
	v_cvt_pk_bf16_f32 v150, v62, v63
	v_pk_mul_f32 v[62:63], v[138:139], v[66:67]
	s_nop 0
	v_cvt_pk_bf16_f32 v151, v62, v63
	ds_read_b128 v[90:93], v112 offset:36928
	ds_read_b128 v[136:139], v112 offset:41536
	ds_read_b128 v[152:155], v112 offset:46144
	ds_read_b128 v[156:159], v112 offset:50752
	ds_read_b128 v[160:163], v112 offset:55360
	ds_read_b128 v[224:227], v112 offset:59968
	ds_read_b128 v[228:231], v112 offset:64576
	ds_read_b128 v[232:235], v113 offset:32320
	ds_read_b128 v[62:65], v123
	ds_read_b128 v[66:69], v123 offset:64
	s_waitcnt lgkmcnt(14)
	v_mfma_f32_16x16x32_bf16 v[144:147], v[192:195], v[140:143], v[144:147]
	v_mfma_f32_16x16x32_bf16 v[164:167], v[196:199], v[140:143], v[164:167]
	v_mfma_f32_16x16x32_bf16 v[168:171], v[200:203], v[140:143], v[168:171]
	v_mfma_f32_16x16x32_bf16 v[172:175], v[204:207], v[140:143], v[172:175]
	s_waitcnt lgkmcnt(13)
	v_mfma_f32_16x16x32_bf16 v[176:179], v[208:211], v[140:143], v[176:179]
	s_waitcnt lgkmcnt(12)
	v_mfma_f32_16x16x32_bf16 v[180:183], v[212:215], v[140:143], v[180:183]
	s_waitcnt lgkmcnt(11)
	v_mfma_f32_16x16x32_bf16 v[184:187], v[216:219], v[140:143], v[184:187]
	s_waitcnt lgkmcnt(10)
	v_mfma_f32_16x16x32_bf16 v[140:143], v[220:223], v[140:143], v[188:191]
	s_nop 2
	ds_read_b128 v[188:191], v112 offset:36992
	ds_read_b128 v[192:195], v112 offset:41600
	ds_read_b128 v[196:199], v112 offset:46208
	ds_read_b128 v[200:203], v112 offset:50816
	ds_read_b128 v[204:207], v112 offset:55424
	ds_read_b128 v[208:211], v112 offset:60032
	ds_read_b128 v[212:215], v112 offset:64640
	ds_read_b128 v[216:219], v113 offset:32384
	ds_read_b128 v[70:73], v123 offset:128
	ds_read_b128 v[78:81], v123 offset:192
	s_waitcnt lgkmcnt(14)
	v_mfma_f32_16x16x32_bf16 v[144:147], v[90:93], v[86:89], v[144:147]
	v_mfma_f32_16x16x32_bf16 v[136:139], v[136:139], v[86:89], v[164:167]
	v_mfma_f32_16x16x32_bf16 v[152:155], v[152:155], v[86:89], v[168:171]
	v_mfma_f32_16x16x32_bf16 v[156:159], v[156:159], v[86:89], v[172:175]
	v_mfma_f32_16x16x32_bf16 v[160:163], v[160:163], v[86:89], v[176:179]
	v_mfma_f32_16x16x32_bf16 v[164:167], v[224:227], v[86:89], v[180:183]
	s_waitcnt lgkmcnt(13)
	v_mfma_f32_16x16x32_bf16 v[168:171], v[228:231], v[86:89], v[184:187]
	s_waitcnt lgkmcnt(12)
	v_mfma_f32_16x16x32_bf16 v[140:143], v[232:235], v[86:89], v[140:143]
	ds_read_b128 v[172:175], v112 offset:37056
	ds_read_b128 v[176:179], v112 offset:41664
	ds_read_b128 v[180:183], v112 offset:46272
	ds_read_b128 v[184:187], v112 offset:50880
	ds_read_b128 v[220:223], v112 offset:55488
	ds_read_b128 v[224:227], v112 offset:60096
	ds_read_b128 v[228:231], v112 offset:64704
	ds_read_b128 v[232:235], v113 offset:32448
	ds_read_b128 v[86:89], v123 offset:256
	ds_read_b128 v[90:93], v123 offset:320
	s_waitcnt lgkmcnt(14)
	v_mfma_f32_16x16x32_bf16 v[144:147], v[188:191], v[148:151], v[144:147]
	v_mfma_f32_16x16x32_bf16 v[136:139], v[192:195], v[148:151], v[136:139]
	v_mfma_f32_16x16x32_bf16 v[152:155], v[196:199], v[148:151], v[152:155]
	v_mfma_f32_16x16x32_bf16 v[156:159], v[200:203], v[148:151], v[156:159]
	v_mfma_f32_16x16x32_bf16 v[160:163], v[204:207], v[148:151], v[160:163]
	v_mfma_f32_16x16x32_bf16 v[164:167], v[208:211], v[148:151], v[164:167]
	s_waitcnt lgkmcnt(13)
	v_mfma_f32_16x16x32_bf16 v[168:171], v[212:215], v[148:151], v[168:171]
	s_waitcnt lgkmcnt(12)
	v_mfma_f32_16x16x32_bf16 v[140:143], v[216:219], v[148:151], v[140:143]
	v_exp_f32_e32 v148, v82
	v_exp_f32_e32 v149, v83
	v_exp_f32_e32 v150, v84
	v_exp_f32_e32 v151, v85
	v_add_f32_e32 v148, 1.0, v148
	v_add_f32_e32 v149, 1.0, v149
	v_rcp_f32_e32 v148, v148
	v_rcp_f32_e32 v149, v149
	v_add_f32_e32 v150, 1.0, v150
	v_add_f32_e32 v151, 1.0, v151
	v_rcp_f32_e32 v150, v150
	v_rcp_f32_e32 v151, v151
	v_pk_mul_f32 v[82:83], v[82:83], v[148:149]
	v_exp_f32_e32 v148, v74
	v_cvt_pk_bf16_f32 v82, v82, v83
	v_pk_mul_f32 v[84:85], v[84:85], v[150:151]
	v_exp_f32_e32 v149, v77
	v_cvt_pk_bf16_f32 v83, v84, v85
	v_exp_f32_e32 v85, v75
	v_add_f32_e32 v84, 1.0, v148
	v_exp_f32_e32 v148, v76
	v_rcp_f32_e32 v84, v84
	v_add_f32_e32 v85, 1.0, v85
	v_rcp_f32_e32 v85, v85
	v_add_f32_e32 v148, 1.0, v148
	v_rcp_f32_e32 v192, v148
	v_add_f32_e32 v148, 1.0, v149
	v_rcp_f32_e32 v193, v148
	ds_read_b128 v[148:151], v123 offset:384
	ds_read_b128 v[188:191], v123 offset:448
	v_pk_mul_f32 v[74:75], v[74:75], v[84:85]
	s_nop 0
	v_cvt_pk_bf16_f32 v84, v74, v75
	v_pk_mul_f32 v[74:75], v[76:77], v[192:193]
	s_nop 0
	v_cvt_pk_bf16_f32 v85, v74, v75
	s_waitcnt lgkmcnt(11)
	s_nop 0
	v_mfma_f32_16x16x32_bf16 v[74:77], v[172:175], v[82:85], v[144:147]
	s_waitcnt lgkmcnt(10)
	v_mfma_f32_16x16x32_bf16 v[136:139], v[176:179], v[82:85], v[136:139]
	s_waitcnt lgkmcnt(9)
	v_mfma_f32_16x16x32_bf16 v[144:147], v[180:183], v[82:85], v[152:155]
	s_waitcnt lgkmcnt(8)
	v_mfma_f32_16x16x32_bf16 v[152:155], v[184:187], v[82:85], v[156:159]
	s_waitcnt lgkmcnt(7)
	v_mfma_f32_16x16x32_bf16 v[156:159], v[220:223], v[82:85], v[160:163]
	s_waitcnt lgkmcnt(6)
	v_mfma_f32_16x16x32_bf16 v[160:163], v[224:227], v[82:85], v[164:167]
	s_waitcnt lgkmcnt(5)
	v_mfma_f32_16x16x32_bf16 v[164:167], v[228:231], v[82:85], v[168:171]
	s_waitcnt lgkmcnt(4)
	v_mfma_f32_16x16x32_bf16 v[82:85], v[232:235], v[82:85], v[140:143]
	s_nop 2
	v_exp_f32_e32 v140, v74
	v_exp_f32_e32 v141, v75
	v_exp_f32_e32 v168, v136
	v_exp_f32_e32 v169, v137
	v_exp_f32_e32 v170, v138
	v_exp_f32_e32 v171, v139
	v_exp_f32_e32 v142, v76
	v_exp_f32_e32 v143, v77
	v_add_f32_e32 v140, 1.0, v140
	v_add_f32_e32 v141, 1.0, v141
	v_rcp_f32_e32 v140, v140
	v_rcp_f32_e32 v141, v141
	v_add_f32_e32 v168, 1.0, v168
	v_add_f32_e32 v169, 1.0, v169
	v_rcp_f32_e32 v168, v168
	v_rcp_f32_e32 v169, v169
	v_pk_add_f32 v[170:171], v[170:171], 1.0 op_sel_hi:[1,0]
	v_pk_add_f32 v[142:143], v[142:143], 1.0 op_sel_hi:[1,0]
	v_rcp_f32_e32 v170, v170
	v_rcp_f32_e32 v171, v171
	v_rcp_f32_e32 v142, v142
	v_rcp_f32_e32 v143, v143
	v_exp_f32_e32 v172, v144
	v_exp_f32_e32 v173, v145
	v_pk_mul_f32 v[74:75], v[74:75], v[140:141]
	v_pk_mul_f32 v[136:137], v[136:137], v[168:169]
	v_pk_fma_f32 v[62:63], v[74:75], s[2:3], v[62:63] op_sel_hi:[1,0,1]
	v_exp_f32_e32 v174, v146
	v_pk_mul_f32 v[236:237], v[62:63], v[62:63]
	v_pk_add_f32 v[238:239], v[62:63], 0 op_sel_hi:[1,0]
	v_exp_f32_e32 v175, v147
	v_pk_fma_f32 v[66:67], v[136:137], s[2:3], v[66:67] op_sel_hi:[1,0,1]
	v_pk_mul_f32 v[136:137], v[138:139], v[170:171]
	v_pk_fma_f32 v[236:237], v[66:67], v[66:67], v[236:237]
	v_pk_add_f32 v[238:239], v[66:67], v[238:239]
	v_pk_fma_f32 v[68:69], v[136:137], s[2:3], v[68:69] op_sel_hi:[1,0,1]
	v_pk_mul_f32 v[74:75], v[76:77], v[142:143]
	v_pk_fma_f32 v[236:237], v[68:69], v[68:69], v[236:237]
	v_pk_add_f32 v[238:239], v[68:69], v[238:239]
	v_pk_add_f32 v[172:173], v[172:173], 1.0 op_sel_hi:[1,0]
	v_exp_f32_e32 v176, v152
	v_exp_f32_e32 v177, v153
	v_pk_fma_f32 v[64:65], v[74:75], s[2:3], v[64:65] op_sel_hi:[1,0,1]
	v_rcp_f32_e32 v172, v172
	v_pk_fma_f32 v[236:237], v[64:65], v[64:65], v[236:237]
	v_pk_add_f32 v[238:239], v[64:65], v[238:239]
	v_rcp_f32_e32 v173, v173
	v_pk_add_f32 v[174:175], v[174:175], 1.0 op_sel_hi:[1,0]
	v_exp_f32_e32 v178, v154
	v_exp_f32_e32 v179, v155
	v_rcp_f32_e32 v174, v174
	v_rcp_f32_e32 v175, v175
	v_pk_add_f32 v[176:177], v[176:177], 1.0 op_sel_hi:[1,0]
	v_exp_f32_e32 v180, v156
	v_exp_f32_e32 v181, v157
	v_rcp_f32_e32 v176, v176
	v_rcp_f32_e32 v177, v177
	v_pk_mul_f32 v[144:145], v[144:145], v[172:173]
	v_pk_add_f32 v[178:179], v[178:179], 1.0 op_sel_hi:[1,0]
	v_exp_f32_e32 v182, v158
	v_exp_f32_e32 v183, v159
	v_pk_fma_f32 v[70:71], v[144:145], s[2:3], v[70:71] op_sel_hi:[1,0,1]
	v_rcp_f32_e32 v178, v178
	v_pk_fma_f32 v[236:237], v[70:71], v[70:71], v[236:237]
	v_pk_add_f32 v[238:239], v[70:71], v[238:239]
	v_rcp_f32_e32 v179, v179
	v_pk_mul_f32 v[144:145], v[146:147], v[174:175]
	v_pk_add_f32 v[180:181], v[180:181], 1.0 op_sel_hi:[1,0]
	v_exp_f32_e32 v184, v160
	v_exp_f32_e32 v185, v161
	v_pk_fma_f32 v[72:73], v[144:145], s[2:3], v[72:73] op_sel_hi:[1,0,1]
	v_rcp_f32_e32 v180, v180
	v_pk_fma_f32 v[236:237], v[72:73], v[72:73], v[236:237]
	v_pk_add_f32 v[238:239], v[72:73], v[238:239]
	v_rcp_f32_e32 v181, v181
	v_pk_mul_f32 v[152:153], v[152:153], v[176:177]
	v_pk_add_f32 v[182:183], v[182:183], 1.0 op_sel_hi:[1,0]
	v_exp_f32_e32 v186, v162
	v_exp_f32_e32 v187, v163
	v_pk_fma_f32 v[78:79], v[152:153], s[2:3], v[78:79] op_sel_hi:[1,0,1]
	v_rcp_f32_e32 v182, v182
	v_pk_fma_f32 v[236:237], v[78:79], v[78:79], v[236:237]
	v_pk_add_f32 v[238:239], v[78:79], v[238:239]
	v_rcp_f32_e32 v183, v183
	v_pk_mul_f32 v[152:153], v[154:155], v[178:179]
	v_pk_add_f32 v[184:185], v[184:185], 1.0 op_sel_hi:[1,0]
	v_exp_f32_e32 v192, v164
	v_exp_f32_e32 v193, v165
	v_pk_fma_f32 v[80:81], v[152:153], s[2:3], v[80:81] op_sel_hi:[1,0,1]
	v_rcp_f32_e32 v184, v184
	v_pk_fma_f32 v[236:237], v[80:81], v[80:81], v[236:237]
	v_pk_add_f32 v[238:239], v[80:81], v[238:239]
	v_rcp_f32_e32 v185, v185
	v_pk_mul_f32 v[156:157], v[156:157], v[180:181]
	v_pk_add_f32 v[186:187], v[186:187], 1.0 op_sel_hi:[1,0]
	v_exp_f32_e32 v194, v166
	v_exp_f32_e32 v195, v167
	s_waitcnt lgkmcnt(3)
	v_pk_fma_f32 v[86:87], v[156:157], s[2:3], v[86:87] op_sel_hi:[1,0,1]
	v_rcp_f32_e32 v186, v186
	v_pk_fma_f32 v[236:237], v[86:87], v[86:87], v[236:237]
	v_pk_add_f32 v[238:239], v[86:87], v[238:239]
	v_rcp_f32_e32 v187, v187
	v_pk_mul_f32 v[156:157], v[158:159], v[182:183]
	v_pk_add_f32 v[192:193], v[192:193], 1.0 op_sel_hi:[1,0]
	v_exp_f32_e32 v196, v82
	v_exp_f32_e32 v197, v83
	v_pk_fma_f32 v[88:89], v[156:157], s[2:3], v[88:89] op_sel_hi:[1,0,1]
	v_rcp_f32_e32 v192, v192
	v_pk_fma_f32 v[236:237], v[88:89], v[88:89], v[236:237]
	v_pk_add_f32 v[238:239], v[88:89], v[238:239]
	v_rcp_f32_e32 v193, v193
	v_pk_mul_f32 v[160:161], v[160:161], v[184:185]
	v_pk_add_f32 v[194:195], v[194:195], 1.0 op_sel_hi:[1,0]
	v_exp_f32_e32 v198, v84
	v_exp_f32_e32 v199, v85
	s_waitcnt lgkmcnt(2)
	v_pk_fma_f32 v[90:91], v[160:161], s[2:3], v[90:91] op_sel_hi:[1,0,1]
	v_rcp_f32_e32 v194, v194
	v_pk_fma_f32 v[236:237], v[90:91], v[90:91], v[236:237]
	v_pk_add_f32 v[238:239], v[90:91], v[238:239]
	v_rcp_f32_e32 v195, v195
	v_pk_mul_f32 v[160:161], v[162:163], v[186:187]
	v_pk_add_f32 v[196:197], v[196:197], 1.0 op_sel_hi:[1,0]
	v_pk_fma_f32 v[92:93], v[160:161], s[2:3], v[92:93] op_sel_hi:[1,0,1]
	v_rcp_f32_e32 v196, v196
	v_pk_fma_f32 v[236:237], v[92:93], v[92:93], v[236:237]
	v_pk_add_f32 v[238:239], v[92:93], v[238:239]
	v_rcp_f32_e32 v197, v197
	v_pk_mul_f32 v[164:165], v[164:165], v[192:193]
	v_pk_add_f32 v[198:199], v[198:199], 1.0 op_sel_hi:[1,0]
	s_waitcnt lgkmcnt(1)
	v_pk_fma_f32 v[148:149], v[164:165], s[2:3], v[148:149] op_sel_hi:[1,0,1]
	v_rcp_f32_e32 v198, v198
	v_pk_fma_f32 v[236:237], v[148:149], v[148:149], v[236:237]
	v_pk_add_f32 v[238:239], v[148:149], v[238:239]
	v_rcp_f32_e32 v199, v199
	v_pk_mul_f32 v[164:165], v[166:167], v[194:195]
	s_nop 0
	v_pk_fma_f32 v[150:151], v[164:165], s[2:3], v[150:151] op_sel_hi:[1,0,1]
	v_pk_mul_f32 v[82:83], v[82:83], v[196:197]
	v_pk_fma_f32 v[236:237], v[150:151], v[150:151], v[236:237]
	v_pk_add_f32 v[238:239], v[150:151], v[238:239]
	s_waitcnt lgkmcnt(0)
	v_pk_fma_f32 v[82:83], v[82:83], s[2:3], v[188:189] op_sel_hi:[1,0,1]
	v_pk_mul_f32 v[84:85], v[84:85], v[198:199]
	v_pk_fma_f32 v[236:237], v[82:83], v[82:83], v[236:237]
	v_pk_fma_f32 v[84:85], v[84:85], s[2:3], v[190:191] op_sel_hi:[1,0,1]
	v_pk_add_f32 v[238:239], v[82:83], v[238:239]
	v_pk_fma_f32 v[236:237], v[84:85], v[84:85], v[236:237]
	v_pk_add_f32 v[238:239], v[84:85], v[238:239]
	v_add_f32_e32 v75, v236, v237
	v_add_f32_e32 v74, v238, v239
	s_nop 1
	v_permlane16_swap_b32_e32 v74, v75
	s_nop 0
	v_add_f32_e32 v74, v74, v75
	v_mov_b32_e32 v75, v74
	s_nop 1
	v_permlane32_swap_b32_e32 v74, v75
	s_nop 0
	v_add_f32_e32 v74, v74, v75
	v_mov_b32_e32 v75, v74
	s_nop 1
	v_permlane16_swap_b32_e32 v74, v75
	s_nop 0
	v_mul_f32_e32 v74, 0x3c000000, v74
	v_mul_f32_e32 v75, 0x3c000000, v75
	v_fma_f32 v75, -v74, v74, v75
	v_add_f32_e32 v75, 0x3727c5ac, v75
	v_rsq_f32_e32 v76, v75
	s_nop 0
	v_mul_f32_e64 v236, -v74, v76
	v_pk_fma_f32 v[62:63], v[62:63], v[76:77], v[236:237] op_sel_hi:[1,0,0]
	v_pk_fma_f32 v[64:65], v[64:65], v[76:77], v[236:237] op_sel_hi:[1,0,0]
	v_pk_fma_f32 v[66:67], v[66:67], v[76:77], v[236:237] op_sel_hi:[1,0,0]
	v_pk_fma_f32 v[68:69], v[68:69], v[76:77], v[236:237] op_sel_hi:[1,0,0]
	ds_write_b128 v123, v[62:65]
	v_pk_fma_f32 v[70:71], v[70:71], v[76:77], v[236:237] op_sel_hi:[1,0,0]
	v_pk_fma_f32 v[72:73], v[72:73], v[76:77], v[236:237] op_sel_hi:[1,0,0]
	ds_write_b128 v123, v[66:69] offset:64
	v_pk_fma_f32 v[78:79], v[78:79], v[76:77], v[236:237] op_sel_hi:[1,0,0]
	v_pk_fma_f32 v[80:81], v[80:81], v[76:77], v[236:237] op_sel_hi:[1,0,0]
	ds_write_b128 v123, v[70:73] offset:128
	v_pk_fma_f32 v[86:87], v[86:87], v[76:77], v[236:237] op_sel_hi:[1,0,0]
	v_pk_fma_f32 v[88:89], v[88:89], v[76:77], v[236:237] op_sel_hi:[1,0,0]
	ds_write_b128 v123, v[78:81] offset:192
	v_pk_fma_f32 v[90:91], v[90:91], v[76:77], v[236:237] op_sel_hi:[1,0,0]
	v_pk_fma_f32 v[92:93], v[92:93], v[76:77], v[236:237] op_sel_hi:[1,0,0]
	ds_write_b128 v123, v[86:89] offset:256
	v_pk_fma_f32 v[148:149], v[148:149], v[76:77], v[236:237] op_sel_hi:[1,0,0]
	v_pk_fma_f32 v[150:151], v[150:151], v[76:77], v[236:237] op_sel_hi:[1,0,0]
	ds_write_b128 v123, v[90:93] offset:320
	v_pk_fma_f32 v[82:83], v[82:83], v[76:77], v[236:237] op_sel_hi:[1,0,0]
	v_pk_fma_f32 v[84:85], v[84:85], v[76:77], v[236:237] op_sel_hi:[1,0,0]
	ds_write_b128 v123, v[148:151] offset:384
	ds_write_b128 v123, v[82:85] offset:448
	ds_read_b128 v[62:65], v121
	ds_read_b128 v[66:69], v121 offset:1088
	ds_read_b128 v[70:73], v121 offset:2176
	ds_read_b128 v[74:77], v121 offset:3264
	ds_read_b128 v[78:81], v121 offset:4352
	ds_read_b128 v[82:85], v121 offset:5440
	ds_read_b128 v[86:89], v121 offset:6528
	ds_read_b128 v[90:93], v121 offset:7616
	v_add_u32_e32 v136, 0xffffe400, v118
	s_waitcnt vmcnt(15) lgkmcnt(7)
	v_pk_fma_f32 v[64:65], v[56:57], v[64:65], v[60:61]
	v_pk_fma_f32 v[62:63], v[54:55], v[62:63], v[58:59]
	buffer_store_dwordx4 v[62:65], v136, s[4:7], 0 offen sc0 nt sc1
	v_cmp_lt_i32_e32 vcc, s8, v0
	s_or_b64 s[0:1], vcc, s[0:1]
	s_waitcnt lgkmcnt(6)
	v_pk_fma_f32 v[64:65], v[56:57], v[68:69], v[60:61]
	v_pk_fma_f32 v[62:63], v[54:55], v[66:67], v[58:59]
	v_add_u32_e32 v66, 0xffffe800, v118
	buffer_store_dwordx4 v[62:65], v66, s[4:7], 0 offen sc0 nt sc1
	v_add_u32_e32 v66, 0xffffec00, v118
	s_waitcnt lgkmcnt(5)
	v_pk_fma_f32 v[64:65], v[56:57], v[72:73], v[60:61]
	v_pk_fma_f32 v[62:63], v[54:55], v[70:71], v[58:59]
	buffer_store_dwordx4 v[62:65], v66, s[4:7], 0 offen sc0 nt sc1
	v_add_u32_e32 v66, 0xfffff000, v118
	s_waitcnt lgkmcnt(4)
	v_pk_fma_f32 v[64:65], v[56:57], v[76:77], v[60:61]
	v_pk_fma_f32 v[62:63], v[54:55], v[74:75], v[58:59]
	buffer_store_dwordx4 v[62:65], v66, s[4:7], 0 offen sc0 nt sc1
	v_add_u32_e32 v66, 0xfffff400, v118
	s_waitcnt lgkmcnt(3)
	v_pk_fma_f32 v[64:65], v[56:57], v[80:81], v[60:61]
	v_pk_fma_f32 v[62:63], v[54:55], v[78:79], v[58:59]
	buffer_store_dwordx4 v[62:65], v66, s[4:7], 0 offen sc0 nt sc1
	v_add_u32_e32 v66, 0xfffff800, v118
	s_waitcnt lgkmcnt(2)
	v_pk_fma_f32 v[64:65], v[56:57], v[84:85], v[60:61]
	v_pk_fma_f32 v[62:63], v[54:55], v[82:83], v[58:59]
	buffer_store_dwordx4 v[62:65], v66, s[4:7], 0 offen sc0 nt sc1
	v_add_u32_e32 v66, 0xfffffc00, v118
	s_waitcnt lgkmcnt(1)
	v_pk_fma_f32 v[64:65], v[56:57], v[88:89], v[60:61]
	v_pk_fma_f32 v[62:63], v[54:55], v[86:87], v[58:59]
	buffer_store_dwordx4 v[62:65], v66, s[4:7], 0 offen sc0 nt sc1
	s_waitcnt lgkmcnt(0)
	s_nop 0
	v_pk_fma_f32 v[64:65], v[56:57], v[92:93], v[60:61]
	v_pk_fma_f32 v[62:63], v[54:55], v[90:91], v[58:59]
	buffer_store_dwordx4 v[62:65], v118, s[4:7], 0 offen sc0 nt sc1
	v_add_u32_e32 v118, 0x1000000, v118
	s_nop 0
	v_mov_b32_e32 v62, v0
	s_waitcnt vmcnt(21)
	v_mov_b32_e32 v64, v135
	s_andn2_b64 exec, exec, s[0:1]
	s_cbranch_execnz .LBB1_6
